# speedup vs baseline: 1.0058x; 1.0058x over previous
.Lq2:
	s_lshl_b32 s60, s50, 4
	v_add_u32_e32 v2, s60, v177
	v_mul_u32_u24_e32 v3, 0x556, v2
	v_lshrrev_b32_e32 v3, 16, v3
	v_mul_u32_u24_e32 v4, 48, v3
	v_sub_u32_e32 v4, v2, v4
	v_mul_u32_u24_e32 v3, 0x6c0, v3
	v_mad_u32_u24 v215, v4, 12, v3
	v_add_u32_e32 v215, v215, v175
	s_lshl_b32 s60, s65, 4
	v_add_u32_e32 v2, s60, v177
	v_mul_u32_u24_e32 v3, 0x556, v2
	v_lshrrev_b32_e32 v3, 16, v3
	v_mul_u32_u24_e32 v4, 48, v3
	v_sub_u32_e32 v4, v2, v4
	v_mul_u32_u24_e32 v3, 0x6c0, v3
	v_mad_u32_u24 v253, v4, 12, v3
	v_add_u32_e32 v253, v253, v175
	s_waitcnt lgkmcnt(0)
	s_cmp_ge_u32 s50, 2
	s_cbranch_scc0 .Lq3
	v_lshrrev_b32_e32 v2, 2, v216
	v_mul_u32_u24_e32 v3, 43, v2
	v_lshrrev_b32_e32 v3, 8, v3
	v_mul_u32_u24_e32 v4, 6, v3
	v_sub_u32_e32 v4, v2, v4
	v_mul_u32_u24_e32 v3, 24, v3
	v_min_u32_e32 v3, 0xa5, v3
	v_lshl_add_u32 v3, v4, 2, v3
	v_lshrrev_b32_e32 v4, 2, v168
	v_add_u32_e32 v3, v3, v4
	v_and_b32_e32 v4, 3, v216
	v_lshlrev_b32_e32 v4, 2, v4
	v_and_b32_e32 v5, 3, v168
	v_or_b32_e32 v4, v4, v5
	v_lshl_or_b32 v252, v3, 4, v4
	v_add_u32_e32 v3, s9, v3
	v_lshlrev_b32_e32 v4, 4, v4
	v_lshl_or_b32 v244, v3, 10, v4
	global_load_dwordx4 v[216:219], v244, s[6:7]
	global_load_dwordx4 v[220:223], v244, s[6:7] offset:256
	global_load_dwordx4 v[224:227], v244, s[6:7] offset:512
	global_load_dwordx4 v[228:231], v244, s[6:7] offset:768
	global_load_dwordx4 v[232:235], v244, s[6:7] offset:2048
	global_load_dwordx4 v[236:239], v244, s[6:7] offset:2304
	global_load_dwordx4 v[240:243], v244, s[6:7] offset:2560
	global_load_dwordx4 v[244:247], v244, s[6:7] offset:2816
	global_load_dwordx4 v[248:251], v248, s[4:5]

.Lq4:
	s_waitcnt vmcnt(9)
	v_mov_b32_e32 v56, 0
	v_mov_b32_e32 v57, 0
	v_dot2c_f32_f16_dpp v56, v210, v178 quad_perm:[0,0,0,0] row_mask:0xf bank_mask:0xf
	v_dot2c_f32_f16_dpp v57, v210, v194 quad_perm:[0,0,0,0] row_mask:0xf bank_mask:0xf
	v_dot2c_f32_f16_dpp v56, v211, v179 quad_perm:[0,0,0,0] row_mask:0xf bank_mask:0xf
	v_dot2c_f32_f16_dpp v57, v211, v195 quad_perm:[0,0,0,0] row_mask:0xf bank_mask:0xf
	v_dot2c_f32_f16_dpp v56, v212, v180 quad_perm:[0,0,0,0] row_mask:0xf bank_mask:0xf
	v_dot2c_f32_f16_dpp v57, v212, v196 quad_perm:[0,0,0,0] row_mask:0xf bank_mask:0xf
	v_dot2c_f32_f16_dpp v56, v213, v181 quad_perm:[0,0,0,0] row_mask:0xf bank_mask:0xf
	v_dot2c_f32_f16_dpp v57, v213, v197 quad_perm:[0,0,0,0] row_mask:0xf bank_mask:0xf
	v_dot2c_f32_f16_dpp v56, v210, v182 quad_perm:[1,1,1,1] row_mask:0xf bank_mask:0xf
	v_dot2c_f32_f16_dpp v57, v210, v198 quad_perm:[1,1,1,1] row_mask:0xf bank_mask:0xf
	v_dot2c_f32_f16_dpp v56, v211, v183 quad_perm:[1,1,1,1] row_mask:0xf bank_mask:0xf
	v_dot2c_f32_f16_dpp v57, v211, v199 quad_perm:[1,1,1,1] row_mask:0xf bank_mask:0xf
	v_dot2c_f32_f16_dpp v56, v212, v184 quad_perm:[1,1,1,1] row_mask:0xf bank_mask:0xf
	v_dot2c_f32_f16_dpp v57, v212, v200 quad_perm:[1,1,1,1] row_mask:0xf bank_mask:0xf
	v_dot2c_f32_f16_dpp v56, v213, v185 quad_perm:[1,1,1,1] row_mask:0xf bank_mask:0xf
	v_dot2c_f32_f16_dpp v57, v213, v201 quad_perm:[1,1,1,1] row_mask:0xf bank_mask:0xf
	v_dot2c_f32_f16_dpp v56, v210, v186 quad_perm:[2,2,2,2] row_mask:0xf bank_mask:0xf
	v_dot2c_f32_f16_dpp v57, v210, v202 quad_perm:[2,2,2,2] row_mask:0xf bank_mask:0xf
	v_dot2c_f32_f16_dpp v56, v211, v187 quad_perm:[2,2,2,2] row_mask:0xf bank_mask:0xf
	v_dot2c_f32_f16_dpp v57, v211, v203 quad_perm:[2,2,2,2] row_mask:0xf bank_mask:0xf
	v_dot2c_f32_f16_dpp v56, v212, v188 quad_perm:[2,2,2,2] row_mask:0xf bank_mask:0xf
	v_dot2c_f32_f16_dpp v57, v212, v204 quad_perm:[2,2,2,2] row_mask:0xf bank_mask:0xf
	v_dot2c_f32_f16_dpp v56, v213, v189 quad_perm:[2,2,2,2] row_mask:0xf bank_mask:0xf
	v_dot2c_f32_f16_dpp v57, v213, v205 quad_perm:[2,2,2,2] row_mask:0xf bank_mask:0xf
	v_dot2c_f32_f16_dpp v56, v210, v190 quad_perm:[3,3,3,3] row_mask:0xf bank_mask:0xf
	v_dot2c_f32_f16_dpp v57, v210, v206 quad_perm:[3,3,3,3] row_mask:0xf bank_mask:0xf
	v_dot2c_f32_f16_dpp v56, v211, v191 quad_perm:[3,3,3,3] row_mask:0xf bank_mask:0xf
	v_dot2c_f32_f16_dpp v57, v211, v207 quad_perm:[3,3,3,3] row_mask:0xf bank_mask:0xf
	v_dot2c_f32_f16_dpp v56, v212, v192 quad_perm:[3,3,3,3] row_mask:0xf bank_mask:0xf
	v_dot2c_f32_f16_dpp v57, v212, v208 quad_perm:[3,3,3,3] row_mask:0xf bank_mask:0xf
	v_dot2c_f32_f16_dpp v56, v213, v193 quad_perm:[3,3,3,3] row_mask:0xf bank_mask:0xf
	v_dot2c_f32_f16_dpp v57, v213, v209 quad_perm:[3,3,3,3] row_mask:0xf bank_mask:0xf
	s_nop 2
	v_and_or_b32 v2, v56, -16, v168
	v_and_or_b32 v3, v57, -16, v176
	v_min_i32_e32 v58, v2, v3
	s_nop 1
	v_min_i32_dpp v58, v58, v58 quad_perm:[1,0,3,2] row_mask:0xf bank_mask:0xf bound_ctrl:1
	s_nop 1
	v_min_i32_dpp v58, v58, v58 quad_perm:[2,3,0,1] row_mask:0xf bank_mask:0xf bound_ctrl:1
	s_nop 1
	v_min_i32_dpp v58, v58, v58 row_half_mirror row_mask:0xf bank_mask:0xf bound_ctrl:1
	v_and_b32_e32 v2, 12, v58
	v_lshlrev_b32_e32 v2, 2, v2
	v_and_b32_e32 v3, 3, v58
	v_sub_u32_e32 v4, v214, v171
	v_add3_u32 v59, v4, v2, v3
	v_cmp_le_u32_e64 s[54:55], s58, v59
	v_cmp_le_u32_e64 s[56:57], s59, v59
	s_nop 1
	v_cndmask_b32_e64 v2, 0, v7, s[54:55]
	v_cndmask_b32_e64 v3, 0, v8, s[56:57]
	v_sub_u32_e32 v4, v59, v2
	v_sub_u32_e32 v4, v4, v3
	v_cndmask_b32_e64 v2, 0, 1, s[54:55]
	v_cndmask_b32_e64 v3, 0, 1, s[56:57]
	v_add_u32_e32 v5, v2, v3
	v_lshlrev_b32_e32 v2, v5, v4
	v_mul_u32_u24_e32 v2, 0xaab, v2
	v_lshrrev_b32_e32 v2, 17, v2
	v_mul_u32_u24_e32 v3, 0x60, v2
	v_lshrrev_b32_e32 v3, v5, v3
	v_add_u32_e32 v3, v4, v3
	v_mul_u32_u24_e32 v3, 12, v3
	v_cndmask_b32_e64 v2, v172, v173, s[54:55]
	v_cndmask_b32_e64 v2, v2, v174, s[56:57]
	v_add_u32_e32 v3, v3, v2
	v_cndmask_b32_e64 v2, v152, v154, s[54:55]
	v_cndmask_b32_e64 v2, v2, v159, s[56:57]
	v_cndmask_b32_e64 v4, v153, v155, s[54:55]
	v_cndmask_b32_e64 v4, v4, v161, s[56:57]
	v_add_co_u32_e64 v60, s[60:61], v2, v3
	s_nop 1
	v_addc_co_u32_e64 v61, s[60:61], 0, v4, s[60:61]
	v_sub_u32_e32 v2, 2, v5
	v_lshlrev_b32_e64 v2, v2, 36
	v_add_u32_e32 v4, 1, v2
	v_mul_u32_u24_e32 v2, v2, v4
	v_lshlrev_b32_e32 v2, 3, v2
	v_add_co_u32_e64 v62, s[60:61], v60, v2
	s_nop 1
	v_addc_co_u32_e64 v63, s[60:61], 0, v61, s[60:61]
	global_load_dwordx3 v[64:66], v[60:61], off
	ds_read_b32 v72, v215
	ds_read_b32 v73, v215 offset:4
	ds_read_b32 v74, v215 offset:8
	s_mov_b64 s[52:53], exec
	s_and_b64 exec, exec, s[48:49]
	global_load_dwordx3 v[68:70], v[62:63], off
	ds_read_b32 v76, v215 offset:11520
	ds_read_b32 v77, v215 offset:11524
	ds_read_b32 v78, v215 offset:11528
	s_mov_b64 exec, s[52:53]
	s_waitcnt vmcnt(2)
	v_mov_b32_e32 v84, 0
	v_mov_b32_e32 v85, 0
	v_dot2c_f32_f16_dpp v84, v248, v216 quad_perm:[0,0,0,0] row_mask:0xf bank_mask:0xf
	v_dot2c_f32_f16_dpp v85, v248, v232 quad_perm:[0,0,0,0] row_mask:0xf bank_mask:0xf
	v_dot2c_f32_f16_dpp v84, v249, v217 quad_perm:[0,0,0,0] row_mask:0xf bank_mask:0xf
	v_dot2c_f32_f16_dpp v85, v249, v233 quad_perm:[0,0,0,0] row_mask:0xf bank_mask:0xf
	v_dot2c_f32_f16_dpp v84, v250, v218 quad_perm:[0,0,0,0] row_mask:0xf bank_mask:0xf
	v_dot2c_f32_f16_dpp v85, v250, v234 quad_perm:[0,0,0,0] row_mask:0xf bank_mask:0xf
	v_dot2c_f32_f16_dpp v84, v251, v219 quad_perm:[0,0,0,0] row_mask:0xf bank_mask:0xf
	v_dot2c_f32_f16_dpp v85, v251, v235 quad_perm:[0,0,0,0] row_mask:0xf bank_mask:0xf
	v_dot2c_f32_f16_dpp v84, v248, v220 quad_perm:[1,1,1,1] row_mask:0xf bank_mask:0xf
	v_dot2c_f32_f16_dpp v85, v248, v236 quad_perm:[1,1,1,1] row_mask:0xf bank_mask:0xf
	v_dot2c_f32_f16_dpp v84, v249, v221 quad_perm:[1,1,1,1] row_mask:0xf bank_mask:0xf
	v_dot2c_f32_f16_dpp v85, v249, v237 quad_perm:[1,1,1,1] row_mask:0xf bank_mask:0xf
	v_dot2c_f32_f16_dpp v84, v250, v222 quad_perm:[1,1,1,1] row_mask:0xf bank_mask:0xf
	v_dot2c_f32_f16_dpp v85, v250, v238 quad_perm:[1,1,1,1] row_mask:0xf bank_mask:0xf
	v_dot2c_f32_f16_dpp v84, v251, v223 quad_perm:[1,1,1,1] row_mask:0xf bank_mask:0xf
	v_dot2c_f32_f16_dpp v85, v251, v239 quad_perm:[1,1,1,1] row_mask:0xf bank_mask:0xf
	v_dot2c_f32_f16_dpp v84, v248, v224 quad_perm:[2,2,2,2] row_mask:0xf bank_mask:0xf
	v_dot2c_f32_f16_dpp v85, v248, v240 quad_perm:[2,2,2,2] row_mask:0xf bank_mask:0xf
	v_dot2c_f32_f16_dpp v84, v249, v225 quad_perm:[2,2,2,2] row_mask:0xf bank_mask:0xf
	v_dot2c_f32_f16_dpp v85, v249, v241 quad_perm:[2,2,2,2] row_mask:0xf bank_mask:0xf
	v_dot2c_f32_f16_dpp v84, v250, v226 quad_perm:[2,2,2,2] row_mask:0xf bank_mask:0xf
	v_dot2c_f32_f16_dpp v85, v250, v242 quad_perm:[2,2,2,2] row_mask:0xf bank_mask:0xf
	v_dot2c_f32_f16_dpp v84, v251, v227 quad_perm:[2,2,2,2] row_mask:0xf bank_mask:0xf
	v_dot2c_f32_f16_dpp v85, v251, v243 quad_perm:[2,2,2,2] row_mask:0xf bank_mask:0xf
	v_dot2c_f32_f16_dpp v84, v248, v228 quad_perm:[3,3,3,3] row_mask:0xf bank_mask:0xf
	v_dot2c_f32_f16_dpp v85, v248, v244 quad_perm:[3,3,3,3] row_mask:0xf bank_mask:0xf
	v_dot2c_f32_f16_dpp v84, v249, v229 quad_perm:[3,3,3,3] row_mask:0xf bank_mask:0xf
	v_dot2c_f32_f16_dpp v85, v249, v245 quad_perm:[3,3,3,3] row_mask:0xf bank_mask:0xf
	v_dot2c_f32_f16_dpp v84, v250, v230 quad_perm:[3,3,3,3] row_mask:0xf bank_mask:0xf
	v_dot2c_f32_f16_dpp v85, v250, v246 quad_perm:[3,3,3,3] row_mask:0xf bank_mask:0xf
	v_dot2c_f32_f16_dpp v84, v251, v231 quad_perm:[3,3,3,3] row_mask:0xf bank_mask:0xf
	v_dot2c_f32_f16_dpp v85, v251, v247 quad_perm:[3,3,3,3] row_mask:0xf bank_mask:0xf
	s_nop 2
	v_and_or_b32 v2, v84, -16, v168
	v_and_or_b32 v3, v85, -16, v176
	v_min_i32_e32 v86, v2, v3
	s_nop 1
	v_min_i32_dpp v86, v86, v86 quad_perm:[1,0,3,2] row_mask:0xf bank_mask:0xf bound_ctrl:1
	s_nop 1
	v_min_i32_dpp v86, v86, v86 quad_perm:[2,3,0,1] row_mask:0xf bank_mask:0xf bound_ctrl:1
	s_nop 1
	v_min_i32_dpp v86, v86, v86 row_half_mirror row_mask:0xf bank_mask:0xf bound_ctrl:1
	v_and_b32_e32 v2, 12, v86
	v_lshlrev_b32_e32 v2, 2, v2
	v_and_b32_e32 v3, 3, v86
	v_sub_u32_e32 v4, v252, v171
	v_add3_u32 v87, v4, v2, v3
	v_cmp_le_u32_e64 s[54:55], s58, v87
	v_cmp_le_u32_e64 s[56:57], s59, v87
	s_nop 1
	v_cndmask_b32_e64 v2, 0, v7, s[54:55]
	v_cndmask_b32_e64 v3, 0, v8, s[56:57]
	v_sub_u32_e32 v4, v87, v2
	v_sub_u32_e32 v4, v4, v3
	v_cndmask_b32_e64 v2, 0, 1, s[54:55]
	v_cndmask_b32_e64 v3, 0, 1, s[56:57]
	v_add_u32_e32 v5, v2, v3
	v_lshlrev_b32_e32 v2, v5, v4
	v_mul_u32_u24_e32 v2, 0xaab, v2
	v_lshrrev_b32_e32 v2, 17, v2
	v_mul_u32_u24_e32 v3, 0x60, v2
	v_lshrrev_b32_e32 v3, v5, v3
	v_add_u32_e32 v3, v4, v3
	v_mul_u32_u24_e32 v3, 12, v3
	v_cndmask_b32_e64 v2, v172, v173, s[54:55]
	v_cndmask_b32_e64 v2, v2, v174, s[56:57]
	v_add_u32_e32 v3, v3, v2
	v_cndmask_b32_e64 v2, v152, v154, s[54:55]
	v_cndmask_b32_e64 v2, v2, v159, s[56:57]
	v_cndmask_b32_e64 v4, v153, v155, s[54:55]
	v_cndmask_b32_e64 v4, v4, v161, s[56:57]
	v_add_co_u32_e64 v88, s[60:61], v2, v3
	s_nop 1
	v_addc_co_u32_e64 v89, s[60:61], 0, v4, s[60:61]
	v_sub_u32_e32 v2, 2, v5
	v_lshlrev_b32_e64 v2, v2, 36
	v_add_u32_e32 v4, 1, v2
	v_mul_u32_u24_e32 v2, v2, v4
	v_lshlrev_b32_e32 v2, 3, v2
	v_add_co_u32_e64 v90, s[60:61], v88, v2
	s_nop 1
	v_addc_co_u32_e64 v91, s[60:61], 0, v89, s[60:61]
	global_load_dwordx3 v[92:94], v[88:89], off
	ds_read_b32 v100, v253
	ds_read_b32 v101, v253 offset:4
	ds_read_b32 v102, v253 offset:8
	s_mov_b64 s[52:53], exec
	s_and_b64 exec, exec, s[48:49]
	global_load_dwordx3 v[96:98], v[90:91], off
	ds_read_b32 v104, v253 offset:11520
	ds_read_b32 v105, v253 offset:11524
	ds_read_b32 v106, v253 offset:11528
	s_mov_b64 exec, s[52:53]
	s_cmp_eq_u32 s50, 0
	s_cbranch_scc0 .Lq5
	s_lshl_b32 s60, s66, 4
	v_add_u32_e32 v2, s60, v177
	v_mul_u32_u24_e32 v3, 0x556, v2
	v_lshrrev_b32_e32 v3, 16, v3
	v_mul_u32_u24_e32 v4, 48, v3
	v_sub_u32_e32 v4, v2, v4
	v_mul_u32_u24_e32 v3, 0x6c0, v3
	v_mad_u32_u24 v53, v4, 12, v3
	v_add_u32_e32 v53, v53, v175
	s_waitcnt vmcnt(4)
	v_mov_b32_e32 v112, 0
	v_mov_b32_e32 v113, 0
	v_dot2c_f32_f16_dpp v112, v48, v16 quad_perm:[0,0,0,0] row_mask:0xf bank_mask:0xf
	v_dot2c_f32_f16_dpp v113, v48, v32 quad_perm:[0,0,0,0] row_mask:0xf bank_mask:0xf
	v_dot2c_f32_f16_dpp v112, v49, v17 quad_perm:[0,0,0,0] row_mask:0xf bank_mask:0xf
	v_dot2c_f32_f16_dpp v113, v49, v33 quad_perm:[0,0,0,0] row_mask:0xf bank_mask:0xf
	v_dot2c_f32_f16_dpp v112, v50, v18 quad_perm:[0,0,0,0] row_mask:0xf bank_mask:0xf
	v_dot2c_f32_f16_dpp v113, v50, v34 quad_perm:[0,0,0,0] row_mask:0xf bank_mask:0xf
	v_dot2c_f32_f16_dpp v112, v51, v19 quad_perm:[0,0,0,0] row_mask:0xf bank_mask:0xf
	v_dot2c_f32_f16_dpp v113, v51, v35 quad_perm:[0,0,0,0] row_mask:0xf bank_mask:0xf
	v_dot2c_f32_f16_dpp v112, v48, v20 quad_perm:[1,1,1,1] row_mask:0xf bank_mask:0xf
	v_dot2c_f32_f16_dpp v113, v48, v36 quad_perm:[1,1,1,1] row_mask:0xf bank_mask:0xf
	v_dot2c_f32_f16_dpp v112, v49, v21 quad_perm:[1,1,1,1] row_mask:0xf bank_mask:0xf
	v_dot2c_f32_f16_dpp v113, v49, v37 quad_perm:[1,1,1,1] row_mask:0xf bank_mask:0xf
	v_dot2c_f32_f16_dpp v112, v50, v22 quad_perm:[1,1,1,1] row_mask:0xf bank_mask:0xf
	v_dot2c_f32_f16_dpp v113, v50, v38 quad_perm:[1,1,1,1] row_mask:0xf bank_mask:0xf
	v_dot2c_f32_f16_dpp v112, v51, v23 quad_perm:[1,1,1,1] row_mask:0xf bank_mask:0xf
	v_dot2c_f32_f16_dpp v113, v51, v39 quad_perm:[1,1,1,1] row_mask:0xf bank_mask:0xf
	v_dot2c_f32_f16_dpp v112, v48, v24 quad_perm:[2,2,2,2] row_mask:0xf bank_mask:0xf
	v_dot2c_f32_f16_dpp v113, v48, v40 quad_perm:[2,2,2,2] row_mask:0xf bank_mask:0xf
	v_dot2c_f32_f16_dpp v112, v49, v25 quad_perm:[2,2,2,2] row_mask:0xf bank_mask:0xf
	v_dot2c_f32_f16_dpp v113, v49, v41 quad_perm:[2,2,2,2] row_mask:0xf bank_mask:0xf
	v_dot2c_f32_f16_dpp v112, v50, v26 quad_perm:[2,2,2,2] row_mask:0xf bank_mask:0xf
	v_dot2c_f32_f16_dpp v113, v50, v42 quad_perm:[2,2,2,2] row_mask:0xf bank_mask:0xf
	v_dot2c_f32_f16_dpp v112, v51, v27 quad_perm:[2,2,2,2] row_mask:0xf bank_mask:0xf
	v_dot2c_f32_f16_dpp v113, v51, v43 quad_perm:[2,2,2,2] row_mask:0xf bank_mask:0xf
	v_dot2c_f32_f16_dpp v112, v48, v28 quad_perm:[3,3,3,3] row_mask:0xf bank_mask:0xf
	v_dot2c_f32_f16_dpp v113, v48, v44 quad_perm:[3,3,3,3] row_mask:0xf bank_mask:0xf
	v_dot2c_f32_f16_dpp v112, v49, v29 quad_perm:[3,3,3,3] row_mask:0xf bank_mask:0xf
	v_dot2c_f32_f16_dpp v113, v49, v45 quad_perm:[3,3,3,3] row_mask:0xf bank_mask:0xf
	v_dot2c_f32_f16_dpp v112, v50, v30 quad_perm:[3,3,3,3] row_mask:0xf bank_mask:0xf
	v_dot2c_f32_f16_dpp v113, v50, v46 quad_perm:[3,3,3,3] row_mask:0xf bank_mask:0xf
	v_dot2c_f32_f16_dpp v112, v51, v31 quad_perm:[3,3,3,3] row_mask:0xf bank_mask:0xf
	v_dot2c_f32_f16_dpp v113, v51, v47 quad_perm:[3,3,3,3] row_mask:0xf bank_mask:0xf
	s_nop 2
	v_and_or_b32 v2, v112, -16, v168
	v_and_or_b32 v3, v113, -16, v176
	v_min_i32_e32 v114, v2, v3
	s_nop 1
	v_min_i32_dpp v114, v114, v114 quad_perm:[1,0,3,2] row_mask:0xf bank_mask:0xf bound_ctrl:1
	s_nop 1
	v_min_i32_dpp v114, v114, v114 quad_perm:[2,3,0,1] row_mask:0xf bank_mask:0xf bound_ctrl:1
	s_nop 1
	v_min_i32_dpp v114, v114, v114 row_half_mirror row_mask:0xf bank_mask:0xf bound_ctrl:1
	v_and_b32_e32 v2, 12, v114
	v_lshlrev_b32_e32 v2, 2, v2
	v_and_b32_e32 v3, 3, v114
	v_sub_u32_e32 v4, v52, v171
	v_add3_u32 v115, v4, v2, v3
	v_cmp_le_u32_e64 s[54:55], s58, v115
	v_cmp_le_u32_e64 s[56:57], s59, v115
	s_nop 1
	v_cndmask_b32_e64 v2, 0, v7, s[54:55]
	v_cndmask_b32_e64 v3, 0, v8, s[56:57]
	v_sub_u32_e32 v4, v115, v2
	v_sub_u32_e32 v4, v4, v3
	v_cndmask_b32_e64 v2, 0, 1, s[54:55]
	v_cndmask_b32_e64 v3, 0, 1, s[56:57]
	v_add_u32_e32 v5, v2, v3
	v_lshlrev_b32_e32 v2, v5, v4
	v_mul_u32_u24_e32 v2, 0xaab, v2
	v_lshrrev_b32_e32 v2, 17, v2
	v_mul_u32_u24_e32 v3, 0x60, v2
	v_lshrrev_b32_e32 v3, v5, v3
	v_add_u32_e32 v3, v4, v3
	v_mul_u32_u24_e32 v3, 12, v3
	v_cndmask_b32_e64 v2, v172, v173, s[54:55]
	v_cndmask_b32_e64 v2, v2, v174, s[56:57]
	v_add_u32_e32 v3, v3, v2
	v_cndmask_b32_e64 v2, v152, v154, s[54:55]
	v_cndmask_b32_e64 v2, v2, v159, s[56:57]
	v_cndmask_b32_e64 v4, v153, v155, s[54:55]
	v_cndmask_b32_e64 v4, v4, v161, s[56:57]
	v_add_co_u32_e64 v116, s[60:61], v2, v3
	s_nop 1
	v_addc_co_u32_e64 v117, s[60:61], 0, v4, s[60:61]
	v_sub_u32_e32 v2, 2, v5
	v_lshlrev_b32_e64 v2, v2, 36
	v_add_u32_e32 v4, 1, v2
	v_mul_u32_u24_e32 v2, v2, v4
	v_lshlrev_b32_e32 v2, 3, v2
	v_add_co_u32_e64 v118, s[60:61], v116, v2
	s_nop 1
	v_addc_co_u32_e64 v119, s[60:61], 0, v117, s[60:61]
	global_load_dwordx3 v[120:122], v[116:117], off
	ds_read_b32 v128, v53
	ds_read_b32 v129, v53 offset:4
	ds_read_b32 v130, v53 offset:8
	s_mov_b64 s[52:53], exec
	s_and_b64 exec, exec, s[48:49]
	global_load_dwordx3 v[124:126], v[118:119], off
	ds_read_b32 v132, v53 offset:11520
	ds_read_b32 v133, v53 offset:11524
	ds_read_b32 v134, v53 offset:11528
	s_mov_b64 exec, s[52:53]
